# E6 plus router fused epilogue: the 8 serialized rinv loads hoisted into one batch with a single wait (4 layer copies)
# baseline (speedup 1.0000x reference)
.LBB0_552:
	s_add_u32 s12, s30, 0x4b200000
	s_waitcnt vmcnt(0)
	s_addc_u32 s13, s31, 0
	s_cmp_eq_u32 s55, 3
	s_barrier
	s_cbranch_scc1 .LBB0_586
	s_lshl_b32 s9, s8, 8
	v_add_u32_e32 v64, s9, v81
	v_mov_b32_e32 v120, v64
	v_ashrrev_i32_e32 v121, 31, v120
	v_lshl_add_u64 v[120:121], v[120:121], 2, s[12:13]
	global_load_dword v104, v[120:121], off
	global_load_dword v106, v[120:121], off offset:64
	global_load_dword v108, v[120:121], off offset:128
	global_load_dword v110, v[120:121], off offset:192
	global_load_dword v112, v[120:121], off offset:512
	global_load_dword v114, v[120:121], off offset:576
	global_load_dword v116, v[120:121], off offset:640
	global_load_dword v118, v[120:121], off offset:704
	s_waitcnt vmcnt(0)
	s_movk_i32 s2, 0x124
	v_lshlrev_b32_e32 v65, 2, v82
	v_mul_lo_u32 v68, v81, s2
	s_movk_i32 s4, 0x48
	v_lshl_or_b32 v65, s55, 5, v65
	v_add_u32_e32 v69, 0, v68
	v_cmp_gt_u32_e32 vcc, s4, v65
	v_lshl_add_u32 v69, v65, 2, v69
	v_mov_b32_e32 v105, v104
	s_and_saveexec_b64 s[2:3], vcc
	s_cbranch_execz .LBB0_555
	v_mov_b32_e32 v70, v104
	v_mov_b32_e32 v71, v104
	v_pk_mul_f32 v[60:61], v[60:61], v[104:105]
	v_pk_mul_f32 v[62:63], v[62:63], v[70:71]
	ds_write2_b32 v69, v60, v61 offset1:1
	ds_write2_b32 v69, v62, v63 offset0:2 offset1:3
.LBB0_555:
	s_or_b64 exec, exec, s[2:3]
	v_or_b32_e32 v60, 16, v65
	v_cmp_gt_u32_e64 s[2:3], s4, v60
	s_and_saveexec_b64 s[4:5], s[2:3]
	s_cbranch_execz .LBB0_557
	v_mov_b32_e32 v60, v104
	v_mov_b32_e32 v61, v104
	v_pk_mul_f32 v[56:57], v[56:57], v[104:105]
	v_pk_mul_f32 v[58:59], v[58:59], v[60:61]
	ds_write2_b32 v69, v56, v57 offset0:16 offset1:17
	ds_write2_b32 v69, v58, v59 offset0:18 offset1:19
.LBB0_557:
	s_or_b64 exec, exec, s[4:5]
	v_add_u32_e32 v58, 0x1240, v68
	v_add_u32_e32 v59, 0, v58
	v_lshl_add_u32 v59, v65, 2, v59
	v_mov_b32_e32 v107, v106
	s_and_saveexec_b64 s[4:5], vcc
	s_cbranch_execz .LBB0_559
	v_mov_b32_e32 v60, v106
	v_mov_b32_e32 v61, v106
	v_pk_mul_f32 v[52:53], v[52:53], v[106:107]
	v_pk_mul_f32 v[54:55], v[54:55], v[60:61]
	ds_write2_b32 v59, v52, v53 offset1:1
	ds_write2_b32 v59, v54, v55 offset0:2 offset1:3
.LBB0_559:
	s_or_b64 exec, exec, s[4:5]
	s_and_saveexec_b64 s[4:5], s[2:3]
	s_cbranch_execz .LBB0_561
	v_mov_b32_e32 v52, v106
	v_mov_b32_e32 v53, v106
	v_pk_mul_f32 v[48:49], v[48:49], v[106:107]
	v_pk_mul_f32 v[50:51], v[50:51], v[52:53]
	ds_write2_b32 v59, v48, v49 offset0:16 offset1:17
	ds_write2_b32 v59, v50, v51 offset0:18 offset1:19
.LBB0_561:
	s_or_b64 exec, exec, s[4:5]
	v_add_u32_e32 v50, 0x1240, v58
	v_add_u32_e32 v51, 0, v50
	v_lshl_add_u32 v51, v65, 2, v51
	v_mov_b32_e32 v109, v108
	s_and_saveexec_b64 s[4:5], vcc
	s_cbranch_execz .LBB0_563
	v_mov_b32_e32 v52, v108
	v_mov_b32_e32 v53, v108
	v_pk_mul_f32 v[44:45], v[44:45], v[108:109]
	v_pk_mul_f32 v[46:47], v[46:47], v[52:53]
	ds_write2_b32 v51, v44, v45 offset1:1
	ds_write2_b32 v51, v46, v47 offset0:2 offset1:3
.LBB0_563:
	s_or_b64 exec, exec, s[4:5]
	s_and_saveexec_b64 s[4:5], s[2:3]
	s_cbranch_execz .LBB0_565
	v_mov_b32_e32 v44, v108
	v_mov_b32_e32 v45, v108
	v_pk_mul_f32 v[40:41], v[40:41], v[108:109]
	v_pk_mul_f32 v[42:43], v[42:43], v[44:45]
	ds_write2_b32 v51, v40, v41 offset0:16 offset1:17
	ds_write2_b32 v51, v42, v43 offset0:18 offset1:19
.LBB0_565:
	s_or_b64 exec, exec, s[4:5]
	v_add_u32_e32 v42, 0x1240, v50
	v_add_u32_e32 v43, 0, v42
	v_lshl_add_u32 v43, v65, 2, v43
	v_mov_b32_e32 v111, v110
	s_and_saveexec_b64 s[4:5], vcc
	s_cbranch_execz .LBB0_567
	v_mov_b32_e32 v44, v110
	v_mov_b32_e32 v45, v110
	v_pk_mul_f32 v[36:37], v[36:37], v[110:111]
	v_pk_mul_f32 v[38:39], v[38:39], v[44:45]
	ds_write2_b32 v43, v36, v37 offset1:1
	ds_write2_b32 v43, v38, v39 offset0:2 offset1:3
.LBB0_567:
	s_or_b64 exec, exec, s[4:5]
	s_and_saveexec_b64 s[4:5], s[2:3]
	s_cbranch_execz .LBB0_569
	v_mov_b32_e32 v36, v110
	v_mov_b32_e32 v37, v110
	v_pk_mul_f32 v[32:33], v[32:33], v[110:111]
	v_pk_mul_f32 v[34:35], v[34:35], v[36:37]
	ds_write2_b32 v43, v32, v33 offset0:16 offset1:17
	ds_write2_b32 v43, v34, v35 offset0:18 offset1:19
.LBB0_569:
	s_or_b64 exec, exec, s[4:5]
	v_add_u32_e32 v34, 0x5b40, v42
	v_add_u32_e32 v35, 0, v34
	v_lshl_add_u32 v35, v65, 2, v35
	v_mov_b32_e32 v113, v112
	s_and_saveexec_b64 s[4:5], vcc
	s_cbranch_execz .LBB0_571
	v_mov_b32_e32 v36, v112
	v_mov_b32_e32 v37, v112
	v_pk_mul_f32 v[28:29], v[28:29], v[112:113]
	v_pk_mul_f32 v[30:31], v[30:31], v[36:37]
	ds_write2_b32 v35, v28, v29 offset1:1
	ds_write2_b32 v35, v30, v31 offset0:2 offset1:3
.LBB0_571:
	s_or_b64 exec, exec, s[4:5]
	s_and_saveexec_b64 s[4:5], s[2:3]
	s_cbranch_execz .LBB0_573
	v_mov_b32_e32 v28, v112
	v_mov_b32_e32 v29, v112
	v_pk_mul_f32 v[24:25], v[24:25], v[112:113]
	v_pk_mul_f32 v[26:27], v[26:27], v[28:29]
	ds_write2_b32 v35, v24, v25 offset0:16 offset1:17
	ds_write2_b32 v35, v26, v27 offset0:18 offset1:19
.LBB0_573:
	s_or_b64 exec, exec, s[4:5]
	v_add_u32_e32 v26, 0x1240, v34
	v_add_u32_e32 v27, 0, v26
	v_lshl_add_u32 v27, v65, 2, v27
	v_mov_b32_e32 v115, v114
	s_and_saveexec_b64 s[4:5], vcc
	s_cbranch_execz .LBB0_575
	v_mov_b32_e32 v28, v114
	v_mov_b32_e32 v29, v114
	v_pk_mul_f32 v[20:21], v[20:21], v[114:115]
	v_pk_mul_f32 v[22:23], v[22:23], v[28:29]
	ds_write2_b32 v27, v20, v21 offset1:1
	ds_write2_b32 v27, v22, v23 offset0:2 offset1:3
.LBB0_575:
	s_or_b64 exec, exec, s[4:5]
	s_and_saveexec_b64 s[4:5], s[2:3]
	s_cbranch_execz .LBB0_577
	v_mov_b32_e32 v20, v114
	v_mov_b32_e32 v21, v114
	v_pk_mul_f32 v[16:17], v[16:17], v[114:115]
	v_pk_mul_f32 v[18:19], v[18:19], v[20:21]
	ds_write2_b32 v27, v16, v17 offset0:16 offset1:17
	ds_write2_b32 v27, v18, v19 offset0:18 offset1:19
.LBB0_577:
	s_or_b64 exec, exec, s[4:5]
	v_add_u32_e32 v117, 0x1240, v26
	v_add_u32_e32 v18, 0, v117
	v_lshl_add_u32 v19, v65, 2, v18
	v_mov_b32_e32 v117, v116
	s_and_saveexec_b64 s[4:5], vcc
	s_cbranch_execz .LBB0_579
	v_mov_b32_e32 v20, v116
	v_mov_b32_e32 v21, v116
	v_pk_mul_f32 v[12:13], v[12:13], v[116:117]
	v_pk_mul_f32 v[14:15], v[14:15], v[20:21]
	ds_write2_b32 v19, v12, v13 offset1:1
	ds_write2_b32 v19, v14, v15 offset0:2 offset1:3
.LBB0_579:
	s_or_b64 exec, exec, s[4:5]
	s_and_saveexec_b64 s[4:5], s[2:3]
	s_cbranch_execz .LBB0_581
	v_mov_b32_e32 v12, v116
	v_mov_b32_e32 v13, v116
	v_pk_mul_f32 v[8:9], v[8:9], v[116:117]
	v_pk_mul_f32 v[10:11], v[10:11], v[12:13]
	ds_write2_b32 v19, v8, v9 offset0:16 offset1:17
	ds_write2_b32 v19, v10, v11 offset0:18 offset1:19
.LBB0_581:
	s_or_b64 exec, exec, s[4:5]
	v_add_u32_e32 v10, 0x1240, v18
	v_lshl_add_u32 v10, v65, 2, v10
	v_mov_b32_e32 v119, v118
	s_and_saveexec_b64 s[4:5], vcc
	s_cbranch_execz .LBB0_583
	v_mov_b32_e32 v12, v118
	v_mov_b32_e32 v13, v118
	v_pk_mul_f32 v[4:5], v[4:5], v[118:119]
	v_pk_mul_f32 v[6:7], v[6:7], v[12:13]
	ds_write2_b32 v10, v4, v5 offset1:1
	ds_write2_b32 v10, v6, v7 offset0:2 offset1:3
.LBB0_583:
	s_or_b64 exec, exec, s[4:5]
	s_and_saveexec_b64 s[4:5], s[2:3]
	s_cbranch_execz .LBB0_585
	v_mov_b32_e32 v4, v118
	v_mov_b32_e32 v5, v118
	v_pk_mul_f32 v[0:1], v[0:1], v[118:119]
	v_pk_mul_f32 v[2:3], v[2:3], v[4:5]
	ds_write2_b32 v10, v0, v1 offset0:16 offset1:17
	ds_write2_b32 v10, v2, v3 offset0:18 offset1:19
